# QKV epilogue: both row halves' sum-of-squares partial loads issued together (one exposed latency per unit instead of two) + final-norm rewrite
# baseline (speedup 1.0000x reference)
.LBB0_1850:
	v_mov_b32_e32 v171, v0
	s_lshl_b32 s15, s18, 8
	v_readfirstlane_b32 s10, v171
	s_ashr_i32 s76, s10, 8
	s_lshl_b32 s13, s76, 6
	v_and_b32_e32 v170, 63, v171
	s_add_i32 s78, s13, s15
	v_or_b32_e32 v130, s78, v170
	v_ashrrev_i32_e32 v131, 31, v130
	v_lshl_add_u64 v[130:131], v[130:131], 2, s[22:23]
	v_add_co_u32_e32 v132, vcc, s70, v130
	global_load_dword v134, v[130:131], off
	s_nop 0
	v_addc_co_u32_e32 v133, vcc, 0, v131, vcc
	global_load_dword v135, v[132:133], off
	v_add_co_u32_e32 v132, vcc, s71, v130
	s_ashr_i32 s10, s10, 6
	s_nop 0
	v_addc_co_u32_e32 v133, vcc, 0, v131, vcc
	global_load_dword v136, v[132:133], off
	v_add_co_u32_e32 v132, vcc, s58, v130
	s_mul_i32 s11, s10, 0xb00
	s_nop 0
	v_addc_co_u32_e32 v133, vcc, 0, v131, vcc
	global_load_dword v137, v[132:133], off
	v_add_co_u32_e32 v132, vcc, s59, v130
	s_add_i32 s19, s11, 0
	s_nop 0
	v_addc_co_u32_e32 v133, vcc, 0, v131, vcc
	global_load_dword v138, v[132:133], off
	v_add_co_u32_e32 v132, vcc, s56, v130
	s_add_i32 s19, s19, 0x20000
	s_nop 0
	v_addc_co_u32_e32 v133, vcc, 0, v131, vcc
	global_load_dword v139, v[132:133], off
	v_add_co_u32_e32 v132, vcc, s97, v130
	s_or_b32 s14, s15, 0x80
	s_nop 0
	v_addc_co_u32_e32 v133, vcc, 0, v131, vcc
	global_load_dword v140, v[132:133], off
	v_add_co_u32_e32 v132, vcc, s4, v130
	s_add_i32 s80, s13, s14
	s_nop 0
	v_addc_co_u32_e32 v133, vcc, 0, v131, vcc
	global_load_dword v141, v[132:133], off
	v_add_co_u32_e32 v132, vcc, s5, v130
	s_and_b32 s49, s10, 3
	s_nop 0
	v_addc_co_u32_e32 v133, vcc, 0, v131, vcc
	global_load_dword v142, v[132:133], off
	v_add_co_u32_e32 v132, vcc, s54, v130
	v_and_b32_e32 v172, 15, v171
	s_nop 0
	v_addc_co_u32_e32 v133, vcc, 0, v131, vcc
	global_load_dword v143, v[132:133], off
	v_add_co_u32_e32 v132, vcc, s55, v130
	s_cmp_gt_i32 s12, 11
	s_nop 0
	v_addc_co_u32_e32 v133, vcc, 0, v131, vcc
	global_load_dword v144, v[132:133], off
	v_add_co_u32_e32 v132, vcc, s61, v130
	s_mov_b64 s[10:11], -1
	s_nop 0
	v_addc_co_u32_e32 v133, vcc, 0, v131, vcc
	global_load_dword v145, v[132:133], off
	v_add_co_u32_e32 v132, vcc, s1, v130
	s_nop 1
	v_addc_co_u32_e32 v133, vcc, 0, v131, vcc
	global_load_dword v154, v[132:133], off
	v_add_co_u32_e32 v132, vcc, s0, v130
	s_nop 1
	v_addc_co_u32_e32 v133, vcc, 0, v131, vcc
	global_load_dword v160, v[132:133], off
	v_add_co_u32_e32 v132, vcc, s62, v130
	s_nop 1
	v_addc_co_u32_e32 v133, vcc, 0, v131, vcc
	v_add_co_u32_e32 v130, vcc, s94, v130
	global_load_dword v132, v[132:133], off
	s_nop 0
	v_addc_co_u32_e32 v131, vcc, 0, v131, vcc
	global_load_dword v130, v[130:131], off
	v_or_b32_e32 v180, s80, v170
	v_ashrrev_i32_e32 v181, 31, v180
	v_lshl_add_u64 v[180:181], v[180:181], 2, s[22:23]
	v_add_co_u32_e32 v182, vcc, s70, v180
	global_load_dword v185, v[180:181], off
	s_nop 0
	v_addc_co_u32_e32 v183, vcc, 0, v181, vcc
	global_load_dword v186, v[182:183], off
	v_add_co_u32_e32 v182, vcc, s71, v180
	s_nop 1
	v_addc_co_u32_e32 v183, vcc, 0, v181, vcc
	global_load_dword v187, v[182:183], off
	v_add_co_u32_e32 v182, vcc, s58, v180
	s_nop 1
	v_addc_co_u32_e32 v183, vcc, 0, v181, vcc
	global_load_dword v188, v[182:183], off
	v_add_co_u32_e32 v182, vcc, s59, v180
	s_nop 1
	v_addc_co_u32_e32 v183, vcc, 0, v181, vcc
	global_load_dword v189, v[182:183], off
	v_add_co_u32_e32 v182, vcc, s56, v180
	s_nop 1
	v_addc_co_u32_e32 v183, vcc, 0, v181, vcc
	global_load_dword v190, v[182:183], off
	v_add_co_u32_e32 v182, vcc, s97, v180
	s_nop 1
	v_addc_co_u32_e32 v183, vcc, 0, v181, vcc
	global_load_dword v191, v[182:183], off
	v_add_co_u32_e32 v182, vcc, s4, v180
	s_nop 1
	v_addc_co_u32_e32 v183, vcc, 0, v181, vcc
	global_load_dword v192, v[182:183], off
	v_add_co_u32_e32 v182, vcc, s5, v180
	s_nop 1
	v_addc_co_u32_e32 v183, vcc, 0, v181, vcc
	global_load_dword v193, v[182:183], off
	v_add_co_u32_e32 v182, vcc, s54, v180
	s_nop 1
	v_addc_co_u32_e32 v183, vcc, 0, v181, vcc
	global_load_dword v194, v[182:183], off
	v_add_co_u32_e32 v182, vcc, s55, v180
	s_nop 1
	v_addc_co_u32_e32 v183, vcc, 0, v181, vcc
	global_load_dword v195, v[182:183], off
	v_add_co_u32_e32 v182, vcc, s61, v180
	s_nop 1
	v_addc_co_u32_e32 v183, vcc, 0, v181, vcc
	global_load_dword v196, v[182:183], off
	v_add_co_u32_e32 v182, vcc, s1, v180
	s_nop 1
	v_addc_co_u32_e32 v183, vcc, 0, v181, vcc
	global_load_dword v197, v[182:183], off
	v_add_co_u32_e32 v182, vcc, s0, v180
	s_nop 1
	v_addc_co_u32_e32 v183, vcc, 0, v181, vcc
	global_load_dword v198, v[182:183], off
	v_add_co_u32_e32 v182, vcc, s62, v180
	s_nop 1
	v_addc_co_u32_e32 v183, vcc, 0, v181, vcc
	v_add_co_u32_e32 v180, vcc, s94, v180
	global_load_dword v182, v[182:183], off
	s_nop 0
	v_addc_co_u32_e32 v181, vcc, 0, v181, vcc
	global_load_dword v180, v[180:181], off
	s_waitcnt vmcnt(16)
	v_add_f32_e32 v131, v134, v135
	v_add_f32_e32 v133, v136, v137
	v_add_f32_e32 v131, v131, v133
	v_add_f32_e32 v134, v138, v139
	v_add_f32_e32 v133, v140, v141
	v_add_f32_e32 v133, v134, v133
	v_add_f32_e32 v131, v131, v133
	v_add_f32_e32 v133, v142, v143
	v_add_f32_e32 v134, v144, v145
	v_add_f32_e32 v133, v133, v134
	v_add_f32_e32 v134, v154, v160
	v_add_f32_e32 v130, v132, v130
	v_add_f32_e32 v130, v134, v130
	v_add_f32_e32 v130, v133, v130
	v_add_f32_e32 v130, v131, v130
	v_fmamk_f32 v130, v130, 0x3a800000, v167
	v_rsq_f32_e32 v130, v130
	v_lshl_add_u32 v134, v170, 2, s19
	ds_write_b32 v134, v130 offset:2304
	s_waitcnt vmcnt(0)
	v_add_f32_e32 v181, v185, v186
	v_add_f32_e32 v183, v187, v188
	v_add_f32_e32 v181, v181, v183
	v_add_f32_e32 v183, v189, v190
	v_add_f32_e32 v185, v191, v192
	v_add_f32_e32 v183, v183, v185
	v_add_f32_e32 v181, v181, v183
	v_add_f32_e32 v183, v193, v194
	v_add_f32_e32 v185, v195, v196
	v_add_f32_e32 v183, v183, v185
	v_add_f32_e32 v185, v197, v198
	v_add_f32_e32 v180, v182, v180
	v_add_f32_e32 v180, v185, v180
	v_add_f32_e32 v180, v183, v180
	v_add_f32_e32 v180, v181, v180
	v_fmamk_f32 v180, v180, 0x3a800000, v167
	v_rsq_f32_e32 v180, v180
	ds_write_b32 v134, v180 offset:2560
	s_cbranch_scc0 .LBB0_1854
	s_cmp_eq_u32 s49, 0
	s_cselect_b64 s[10:11], -1, 0
	v_cmp_gt_u32_e32 vcc, 32, v170
	s_and_b64 s[16:17], s[10:11], vcc
	s_and_saveexec_b64 s[10:11], s[16:17]
	s_cbranch_execz .LBB0_1853
	v_lshlrev_b32_e32 v130, 1, v171
	v_readlane_b32 s16, v254, 30
	v_and_b32_e32 v154, 32, v130
	v_readlane_b32 s17, v254, 31
	s_nop 4
	global_load_dwordx4 v[130:133], v154, s[16:17]
	global_load_dwordx4 v[134:137], v154, s[16:17] offset:16
	v_lshl_add_u32 v138, v172, 2, s19
	v_add_u32_e32 v173, 0x800, v138
	ds_read2_b32 v[162:163], v173 offset0:64 offset1:80
	s_waitcnt lgkmcnt(0)
	v_mul_f32_e32 v142, 0x3d800000, v162
	s_waitcnt vmcnt(0)
	v_pk_fma_f32 v[140:141], v[122:123], v[142:143], v[134:135] op_sel_hi:[1,0,1]
	s_nop 0
	v_min_f32_e32 v144, 0, v140
	v_mul_f32_e64 v140, |v140|, s33
	v_exp_f32_e32 v140, v140
	v_pk_fma_f32 v[138:139], v[124:125], v[142:143], v[136:137] op_sel_hi:[1,0,1]
	v_min_f32_e32 v145, 0, v141
	v_add_f32_e32 v140, 1.0, v140
	v_log_f32_e32 v143, v140
	v_mul_f32_e64 v140, |v141|, s33
	v_exp_f32_e32 v140, v140
	v_min_f32_e32 v141, 0, v139
	v_mul_f32_e64 v139, |v139|, s33
	v_exp_f32_e32 v139, v139
	v_add_f32_e32 v140, 1.0, v140
	v_log_f32_e32 v160, v140
	v_min_f32_e32 v140, 0, v138
	v_mul_f32_e64 v138, |v138|, s33
	v_exp_f32_e32 v138, v138
	v_add_f32_e32 v139, 1.0, v139
	v_log_f32_e32 v139, v139
	v_add_f32_e32 v138, 1.0, v138
	v_log_f32_e32 v138, v138
	v_xor_b32_e32 v139, 0x80000000, v139
	v_xor_b32_e32 v138, 0x80000000, v138
	v_pk_fma_f32 v[140:141], v[138:139], s[46:47], v[140:141] op_sel_hi:[1,0,1]
	v_xor_b32_e32 v139, 0x80000000, v160
	v_xor_b32_e32 v138, 0x80000000, v143
	v_pk_fma_f32 v[138:139], v[138:139], s[46:47], v[144:145] op_sel_hi:[1,0,1]
	v_pk_fma_f32 v[144:145], v[128:129], v[142:143], v[132:133] op_sel_hi:[1,0,1]
	v_pk_fma_f32 v[142:143], v[126:127], v[142:143], v[130:131] op_sel_hi:[1,0,1]
	s_nop 0
	v_min_f32_e32 v160, 0, v142
	v_mul_f32_e64 v142, |v142|, s33
	v_exp_f32_e32 v142, v142
	v_min_f32_e32 v161, 0, v143
	v_add_f32_e32 v142, 1.0, v142
	v_log_f32_e32 v162, v142
	v_mul_f32_e64 v142, |v143|, s33
	v_mul_f32_e64 v143, |v144|, s33
	v_exp_f32_e32 v142, v142
	v_exp_f32_e32 v143, v143
	v_add_f32_e32 v142, 1.0, v142
	v_add_f32_e32 v143, 1.0, v143
	v_log_f32_e32 v174, v142
	v_min_f32_e32 v142, 0, v144
	v_log_f32_e32 v144, v143
	v_min_f32_e32 v143, 0, v145
	v_mul_f32_e64 v145, |v145|, s33
	v_exp_f32_e32 v145, v145
	v_xor_b32_e32 v144, 0x80000000, v144
	v_add_f32_e32 v145, 1.0, v145
	v_log_f32_e32 v145, v145
	s_nop 0
	v_xor_b32_e32 v145, 0x80000000, v145
	v_pk_fma_f32 v[144:145], v[144:145], s[46:47], v[142:143] op_sel_hi:[1,0,1]
	v_xor_b32_e32 v143, 0x80000000, v174
	v_xor_b32_e32 v142, 0x80000000, v162
	v_pk_fma_f32 v[142:143], v[142:143], s[46:47], v[160:161] op_sel_hi:[1,0,1]
	v_or_b32_e32 v160, s15, v172
	v_add_u32_e32 v160, s13, v160
	v_ashrrev_i32_e32 v161, 31, v160
	v_lshlrev_b64 v[174:175], 6, v[160:161]
	v_lshl_add_u64 v[174:175], s[24:25], 0, v[174:175]
	v_lshl_add_u64 v[174:175], v[174:175], 0, v[154:155]
	global_store_dwordx4 v[174:175], v[142:145], off
	global_store_dwordx4 v[174:175], v[138:141], off offset:16
	s_nop 1
	v_mul_f32_e32 v138, 0x3d800000, v163
	v_pk_fma_f32 v[144:145], v[106:107], v[138:139], v[134:135] op_sel_hi:[1,0,1]
	v_pk_fma_f32 v[142:143], v[108:109], v[138:139], v[136:137] op_sel_hi:[1,0,1]
	v_min_f32_e32 v140, 0, v144
	v_mul_f32_e64 v139, |v144|, s33
	v_mul_f32_e64 v144, |v145|, s33
	v_exp_f32_e32 v144, v144
	v_min_f32_e32 v141, 0, v145
	v_min_f32_e32 v145, 0, v143
	v_mul_f32_e64 v143, |v143|, s33
	v_add_f32_e32 v144, 1.0, v144
	v_log_f32_e32 v161, v144
	v_min_f32_e32 v144, 0, v142
	v_mul_f32_e64 v142, |v142|, s33
	v_exp_f32_e32 v142, v142
	v_exp_f32_e32 v143, v143
	v_exp_f32_e32 v139, v139
	v_add_f32_e32 v142, 1.0, v142
	v_add_f32_e32 v143, 1.0, v143
	v_add_f32_e32 v139, 1.0, v139
	v_log_f32_e32 v142, v142
	v_log_f32_e32 v143, v143
	v_log_f32_e32 v139, v139
	v_xor_b32_e32 v142, 0x80000000, v142
	v_xor_b32_e32 v143, 0x80000000, v143
	v_pk_fma_f32 v[142:143], v[142:143], s[46:47], v[144:145] op_sel_hi:[1,0,1]
	v_xor_b32_e32 v145, 0x80000000, v161
	v_xor_b32_e32 v144, 0x80000000, v139
	v_pk_fma_f32 v[140:141], v[144:145], s[46:47], v[140:141] op_sel_hi:[1,0,1]
	v_pk_fma_f32 v[144:145], v[112:113], v[138:139], v[132:133] op_sel_hi:[1,0,1]
	v_pk_fma_f32 v[138:139], v[110:111], v[138:139], v[130:131] op_sel_hi:[1,0,1]
	s_nop 0
	v_min_f32_e32 v162, 0, v138
	v_mul_f32_e64 v138, |v138|, s33
	v_exp_f32_e32 v138, v138
	v_min_f32_e32 v163, 0, v139
	v_add_f32_e32 v138, 1.0, v138
	v_log_f32_e32 v161, v138
	v_mul_f32_e64 v138, |v139|, s33
	v_mul_f32_e64 v139, |v144|, s33
	v_exp_f32_e32 v138, v138
	v_exp_f32_e32 v139, v139
	v_add_f32_e32 v138, 1.0, v138
	v_add_f32_e32 v139, 1.0, v139
	v_log_f32_e32 v174, v138
	v_min_f32_e32 v138, 0, v144
	v_log_f32_e32 v144, v139
	v_min_f32_e32 v139, 0, v145
	v_mul_f32_e64 v145, |v145|, s33
	v_exp_f32_e32 v145, v145
	v_xor_b32_e32 v144, 0x80000000, v144
	v_add_f32_e32 v145, 1.0, v145
	v_log_f32_e32 v145, v145
	s_nop 0
	v_xor_b32_e32 v145, 0x80000000, v145
	v_pk_fma_f32 v[176:177], v[144:145], s[46:47], v[138:139] op_sel_hi:[1,0,1]
	v_xor_b32_e32 v139, 0x80000000, v174
	v_xor_b32_e32 v138, 0x80000000, v161
	v_pk_fma_f32 v[174:175], v[138:139], s[46:47], v[162:163] op_sel_hi:[1,0,1]
	v_add_u32_e32 v138, 16, v160
	v_ashrrev_i32_e32 v139, 31, v138
	v_lshlrev_b64 v[138:139], 6, v[138:139]
	v_lshl_add_u64 v[138:139], s[24:25], 0, v[138:139]
	v_lshl_add_u64 v[138:139], v[138:139], 0, v[154:155]
	global_store_dwordx4 v[138:139], v[174:177], off
	global_store_dwordx4 v[138:139], v[140:143], off offset:16
	ds_read2_b32 v[138:139], v173 offset0:96 offset1:112
	s_waitcnt lgkmcnt(0)
	v_mul_f32_e32 v138, 0x3d800000, v138
	v_pk_fma_f32 v[142:143], v[90:91], v[138:139], v[134:135] op_sel_hi:[1,0,1]
	v_pk_fma_f32 v[140:141], v[92:93], v[138:139], v[136:137] op_sel_hi:[1,0,1]
	v_min_f32_e32 v144, 0, v142
	v_mul_f32_e64 v142, |v142|, s33
	v_exp_f32_e32 v142, v142
	v_min_f32_e32 v145, 0, v143
	v_add_f32_e32 v142, 1.0, v142
	v_log_f32_e32 v161, v142
	v_mul_f32_e64 v142, |v143|, s33
	v_exp_f32_e32 v142, v142
	v_min_f32_e32 v143, 0, v141
	v_mul_f32_e64 v141, |v141|, s33
	v_exp_f32_e32 v141, v141
	v_add_f32_e32 v142, 1.0, v142
	v_log_f32_e32 v162, v142
	v_min_f32_e32 v142, 0, v140
	v_mul_f32_e64 v140, |v140|, s33
	v_exp_f32_e32 v140, v140
	v_add_f32_e32 v141, 1.0, v141
	v_log_f32_e32 v141, v141
	v_add_f32_e32 v140, 1.0, v140
	v_log_f32_e32 v140, v140
	v_xor_b32_e32 v141, 0x80000000, v141
	v_xor_b32_e32 v140, 0x80000000, v140
	v_pk_fma_f32 v[142:143], v[140:141], s[46:47], v[142:143] op_sel_hi:[1,0,1]
	v_xor_b32_e32 v141, 0x80000000, v162
	v_xor_b32_e32 v140, 0x80000000, v161
	v_pk_fma_f32 v[140:141], v[140:141], s[46:47], v[144:145] op_sel_hi:[1,0,1]
	v_pk_fma_f32 v[144:145], v[96:97], v[138:139], v[132:133] op_sel_hi:[1,0,1]
	v_pk_fma_f32 v[162:163], v[94:95], v[138:139], v[130:131] op_sel_hi:[1,0,1]
	s_nop 0
	v_min_f32_e32 v174, 0, v162
	v_mul_f32_e64 v138, |v162|, s33
	v_min_f32_e32 v175, 0, v163
	v_mul_f32_e64 v161, |v163|, s33
	v_min_f32_e32 v162, 0, v144
	v_mul_f32_e64 v144, |v144|, s33
	v_min_f32_e32 v163, 0, v145
	v_mul_f32_e64 v145, |v145|, s33
	v_exp_f32_e32 v144, v144
	v_exp_f32_e32 v145, v145
	v_exp_f32_e32 v138, v138
	v_exp_f32_e32 v161, v161
	v_add_f32_e32 v144, 1.0, v144
	v_add_f32_e32 v145, 1.0, v145
	v_add_f32_e32 v138, 1.0, v138
	v_add_f32_e32 v161, 1.0, v161
	v_log_f32_e32 v144, v144
	v_log_f32_e32 v145, v145
	v_log_f32_e32 v138, v138
	v_log_f32_e32 v161, v161
	v_xor_b32_e32 v144, 0x80000000, v144
	v_xor_b32_e32 v145, 0x80000000, v145
	v_pk_fma_f32 v[176:177], v[144:145], s[46:47], v[162:163] op_sel_hi:[1,0,1]
	v_xor_b32_e32 v145, 0x80000000, v161
	v_xor_b32_e32 v144, 0x80000000, v138
	v_pk_fma_f32 v[174:175], v[144:145], s[46:47], v[174:175] op_sel_hi:[1,0,1]
	v_add_u32_e32 v144, 32, v160
	v_ashrrev_i32_e32 v145, 31, v144
	v_lshlrev_b64 v[144:145], 6, v[144:145]
	v_lshl_add_u64 v[144:145], s[24:25], 0, v[144:145]
	v_lshl_add_u64 v[144:145], v[144:145], 0, v[154:155]
	global_store_dwordx4 v[144:145], v[174:177], off
	global_store_dwordx4 v[144:145], v[140:143], off offset:16
	s_nop 1
	v_mul_f32_e32 v142, 0x3d800000, v139
	v_pk_fma_f32 v[140:141], v[74:75], v[142:143], v[134:135] op_sel_hi:[1,0,1]
	v_pk_fma_f32 v[138:139], v[76:77], v[142:143], v[136:137] op_sel_hi:[1,0,1]
	v_min_f32_e32 v144, 0, v140
	v_mul_f32_e64 v140, |v140|, s33
	v_exp_f32_e32 v140, v140
	v_min_f32_e32 v145, 0, v141
	v_add_f32_e32 v140, 1.0, v140
	v_log_f32_e32 v143, v140
	v_mul_f32_e64 v140, |v141|, s33
	v_exp_f32_e32 v140, v140
	v_min_f32_e32 v141, 0, v139
	v_mul_f32_e64 v139, |v139|, s33
	v_exp_f32_e32 v139, v139
	v_add_f32_e32 v140, 1.0, v140
	v_log_f32_e32 v161, v140
	v_min_f32_e32 v140, 0, v138
	v_mul_f32_e64 v138, |v138|, s33
	v_exp_f32_e32 v138, v138
	v_add_f32_e32 v139, 1.0, v139
	v_log_f32_e32 v139, v139
	v_add_f32_e32 v138, 1.0, v138
	v_log_f32_e32 v138, v138
	v_xor_b32_e32 v139, 0x80000000, v139
	v_xor_b32_e32 v138, 0x80000000, v138
	v_pk_fma_f32 v[140:141], v[138:139], s[46:47], v[140:141] op_sel_hi:[1,0,1]
	v_xor_b32_e32 v139, 0x80000000, v161
	v_xor_b32_e32 v138, 0x80000000, v143
	v_pk_fma_f32 v[138:139], v[138:139], s[46:47], v[144:145] op_sel_hi:[1,0,1]
	v_pk_fma_f32 v[144:145], v[80:81], v[142:143], v[132:133] op_sel_hi:[1,0,1]
	v_pk_fma_f32 v[142:143], v[78:79], v[142:143], v[130:131] op_sel_hi:[1,0,1]
	s_nop 0
	v_min_f32_e32 v162, 0, v142
	v_mul_f32_e64 v142, |v142|, s33
	v_exp_f32_e32 v142, v142
	v_min_f32_e32 v163, 0, v143
	v_add_f32_e32 v142, 1.0, v142
	v_log_f32_e32 v161, v142
	v_mul_f32_e64 v142, |v143|, s33
	v_mul_f32_e64 v143, |v144|, s33
	v_exp_f32_e32 v142, v142
	v_exp_f32_e32 v143, v143
	v_add_f32_e32 v142, 1.0, v142
	v_add_f32_e32 v143, 1.0, v143
	v_log_f32_e32 v174, v142
	v_min_f32_e32 v142, 0, v144
	v_log_f32_e32 v144, v143
	v_min_f32_e32 v143, 0, v145
	v_mul_f32_e64 v145, |v145|, s33
	v_exp_f32_e32 v145, v145
	v_xor_b32_e32 v144, 0x80000000, v144
	v_add_f32_e32 v145, 1.0, v145
	v_log_f32_e32 v145, v145
	s_nop 0
	v_xor_b32_e32 v145, 0x80000000, v145
	v_pk_fma_f32 v[144:145], v[144:145], s[46:47], v[142:143] op_sel_hi:[1,0,1]
	v_xor_b32_e32 v143, 0x80000000, v174
	v_xor_b32_e32 v142, 0x80000000, v161
	v_pk_fma_f32 v[142:143], v[142:143], s[46:47], v[162:163] op_sel_hi:[1,0,1]
	v_add_u32_e32 v162, 48, v160
	v_ashrrev_i32_e32 v163, 31, v162
	v_lshlrev_b64 v[162:163], 6, v[162:163]
	v_lshl_add_u64 v[162:163], s[24:25], 0, v[162:163]
	v_lshl_add_u64 v[162:163], v[162:163], 0, v[154:155]
	global_store_dwordx4 v[162:163], v[142:145], off
	global_store_dwordx4 v[162:163], v[138:141], off offset:16
	ds_read2_b32 v[138:139], v173 offset0:128 offset1:144
	s_waitcnt lgkmcnt(0)
	v_mul_f32_e32 v138, 0x3d800000, v138
	v_pk_fma_f32 v[142:143], v[58:59], v[138:139], v[134:135] op_sel_hi:[1,0,1]
	v_pk_fma_f32 v[140:141], v[60:61], v[138:139], v[136:137] op_sel_hi:[1,0,1]
	v_min_f32_e32 v144, 0, v142
	v_mul_f32_e64 v142, |v142|, s33
	v_exp_f32_e32 v142, v142
	v_min_f32_e32 v145, 0, v143
	v_add_f32_e32 v142, 1.0, v142
	v_log_f32_e32 v161, v142
	v_mul_f32_e64 v142, |v143|, s33
	v_exp_f32_e32 v142, v142
	v_min_f32_e32 v143, 0, v141
	v_mul_f32_e64 v141, |v141|, s33
	v_exp_f32_e32 v141, v141
	v_add_f32_e32 v142, 1.0, v142
	v_log_f32_e32 v162, v142
	v_min_f32_e32 v142, 0, v140
	v_mul_f32_e64 v140, |v140|, s33
	v_exp_f32_e32 v140, v140
	v_add_f32_e32 v141, 1.0, v141
	v_log_f32_e32 v141, v141
	v_add_f32_e32 v140, 1.0, v140
	v_log_f32_e32 v140, v140
	v_xor_b32_e32 v141, 0x80000000, v141
	v_xor_b32_e32 v140, 0x80000000, v140
	v_pk_fma_f32 v[142:143], v[140:141], s[46:47], v[142:143] op_sel_hi:[1,0,1]
	v_xor_b32_e32 v141, 0x80000000, v162
	v_xor_b32_e32 v140, 0x80000000, v161
	v_pk_fma_f32 v[140:141], v[140:141], s[46:47], v[144:145] op_sel_hi:[1,0,1]
	v_pk_fma_f32 v[144:145], v[64:65], v[138:139], v[132:133] op_sel_hi:[1,0,1]
	v_pk_fma_f32 v[162:163], v[62:63], v[138:139], v[130:131] op_sel_hi:[1,0,1]
	s_nop 0
	v_min_f32_e32 v174, 0, v162
	v_mul_f32_e64 v138, |v162|, s33
	v_min_f32_e32 v175, 0, v163
	v_mul_f32_e64 v161, |v163|, s33
	v_min_f32_e32 v162, 0, v144
	v_mul_f32_e64 v144, |v144|, s33
	v_min_f32_e32 v163, 0, v145
	v_mul_f32_e64 v145, |v145|, s33
	v_exp_f32_e32 v144, v144
	v_exp_f32_e32 v145, v145
	v_exp_f32_e32 v138, v138
	v_exp_f32_e32 v161, v161
	v_add_f32_e32 v144, 1.0, v144
	v_add_f32_e32 v145, 1.0, v145
	v_add_f32_e32 v138, 1.0, v138
	v_add_f32_e32 v161, 1.0, v161
	v_log_f32_e32 v144, v144
	v_log_f32_e32 v145, v145
	v_log_f32_e32 v138, v138
	v_log_f32_e32 v161, v161
	v_xor_b32_e32 v144, 0x80000000, v144
	v_xor_b32_e32 v145, 0x80000000, v145
	v_pk_fma_f32 v[176:177], v[144:145], s[46:47], v[162:163] op_sel_hi:[1,0,1]
	v_xor_b32_e32 v145, 0x80000000, v161
	v_xor_b32_e32 v144, 0x80000000, v138
	v_or_b32_e32 v138, s14, v172
	v_pk_fma_f32 v[174:175], v[144:145], s[46:47], v[174:175] op_sel_hi:[1,0,1]
	v_add_u32_e32 v144, s13, v138
	v_ashrrev_i32_e32 v145, 31, v144
	v_lshlrev_b64 v[144:145], 6, v[144:145]
	v_lshl_add_u64 v[144:145], s[24:25], 0, v[144:145]
	v_lshl_add_u64 v[144:145], v[144:145], 0, v[154:155]
	global_store_dwordx4 v[144:145], v[174:177], off
	global_store_dwordx4 v[144:145], v[140:143], off offset:16
	s_nop 1
	v_mul_f32_e32 v142, 0x3d800000, v139
	v_pk_fma_f32 v[140:141], v[42:43], v[142:143], v[134:135] op_sel_hi:[1,0,1]
	v_pk_fma_f32 v[138:139], v[44:45], v[142:143], v[136:137] op_sel_hi:[1,0,1]
	v_min_f32_e32 v144, 0, v140
	v_mul_f32_e64 v140, |v140|, s33
	v_exp_f32_e32 v140, v140
	v_min_f32_e32 v145, 0, v141
	v_add_f32_e32 v140, 1.0, v140
	v_log_f32_e32 v143, v140
	v_mul_f32_e64 v140, |v141|, s33
	v_exp_f32_e32 v140, v140
	v_min_f32_e32 v141, 0, v139
	v_mul_f32_e64 v139, |v139|, s33
	v_exp_f32_e32 v139, v139
	v_add_f32_e32 v140, 1.0, v140
	v_log_f32_e32 v161, v140
	v_min_f32_e32 v140, 0, v138
	v_mul_f32_e64 v138, |v138|, s33
	v_exp_f32_e32 v138, v138
	v_add_f32_e32 v139, 1.0, v139
	v_log_f32_e32 v139, v139
	v_add_f32_e32 v138, 1.0, v138
	v_log_f32_e32 v138, v138
	v_xor_b32_e32 v139, 0x80000000, v139
	v_xor_b32_e32 v138, 0x80000000, v138
	v_pk_fma_f32 v[140:141], v[138:139], s[46:47], v[140:141] op_sel_hi:[1,0,1]
	v_xor_b32_e32 v139, 0x80000000, v161
	v_xor_b32_e32 v138, 0x80000000, v143
	v_pk_fma_f32 v[138:139], v[138:139], s[46:47], v[144:145] op_sel_hi:[1,0,1]
	v_pk_fma_f32 v[144:145], v[48:49], v[142:143], v[132:133] op_sel_hi:[1,0,1]
	v_pk_fma_f32 v[142:143], v[46:47], v[142:143], v[130:131] op_sel_hi:[1,0,1]
	s_nop 0
	v_min_f32_e32 v162, 0, v142
	v_mul_f32_e64 v142, |v142|, s33
	v_exp_f32_e32 v142, v142
	v_min_f32_e32 v163, 0, v143
	v_add_f32_e32 v142, 1.0, v142
	v_log_f32_e32 v161, v142
	v_mul_f32_e64 v142, |v143|, s33
	v_mul_f32_e64 v143, |v144|, s33
	v_exp_f32_e32 v142, v142
	v_exp_f32_e32 v143, v143
	v_add_f32_e32 v142, 1.0, v142
	v_add_f32_e32 v143, 1.0, v143
	v_log_f32_e32 v174, v142
	v_min_f32_e32 v142, 0, v144
	v_log_f32_e32 v144, v143
	v_min_f32_e32 v143, 0, v145
	v_mul_f32_e64 v145, |v145|, s33
	v_exp_f32_e32 v145, v145
	v_xor_b32_e32 v144, 0x80000000, v144
	v_add_f32_e32 v145, 1.0, v145
	v_log_f32_e32 v145, v145
	s_nop 0
	v_xor_b32_e32 v145, 0x80000000, v145
	v_pk_fma_f32 v[144:145], v[144:145], s[46:47], v[142:143] op_sel_hi:[1,0,1]
	v_xor_b32_e32 v143, 0x80000000, v174
	v_xor_b32_e32 v142, 0x80000000, v161
	v_pk_fma_f32 v[142:143], v[142:143], s[46:47], v[162:163] op_sel_hi:[1,0,1]
	v_add_u32_e32 v162, 0x90, v160
	v_ashrrev_i32_e32 v163, 31, v162
	v_lshlrev_b64 v[162:163], 6, v[162:163]
	v_lshl_add_u64 v[162:163], s[24:25], 0, v[162:163]
	v_lshl_add_u64 v[162:163], v[162:163], 0, v[154:155]
	global_store_dwordx4 v[162:163], v[142:145], off
	global_store_dwordx4 v[162:163], v[138:141], off offset:16
	ds_read2_b32 v[138:139], v173 offset0:160 offset1:176
	s_waitcnt lgkmcnt(0)
	v_mul_f32_e32 v138, 0x3d800000, v138
	v_pk_fma_f32 v[142:143], v[26:27], v[138:139], v[134:135] op_sel_hi:[1,0,1]
	v_pk_fma_f32 v[140:141], v[28:29], v[138:139], v[136:137] op_sel_hi:[1,0,1]
	v_min_f32_e32 v144, 0, v142
	v_mul_f32_e64 v142, |v142|, s33
	v_exp_f32_e32 v142, v142
	v_min_f32_e32 v145, 0, v143
	v_add_f32_e32 v142, 1.0, v142
	v_log_f32_e32 v161, v142
	v_mul_f32_e64 v142, |v143|, s33
	v_exp_f32_e32 v142, v142
	v_min_f32_e32 v143, 0, v141
	v_mul_f32_e64 v141, |v141|, s33
	v_exp_f32_e32 v141, v141
	v_add_f32_e32 v142, 1.0, v142
	v_log_f32_e32 v162, v142
	v_min_f32_e32 v142, 0, v140
	v_mul_f32_e64 v140, |v140|, s33
	v_exp_f32_e32 v140, v140
	v_add_f32_e32 v141, 1.0, v141
	v_log_f32_e32 v141, v141
	v_add_f32_e32 v140, 1.0, v140
	v_log_f32_e32 v140, v140
	v_xor_b32_e32 v141, 0x80000000, v141
	v_xor_b32_e32 v140, 0x80000000, v140
	v_pk_fma_f32 v[142:143], v[140:141], s[46:47], v[142:143] op_sel_hi:[1,0,1]
	v_xor_b32_e32 v141, 0x80000000, v162
	v_xor_b32_e32 v140, 0x80000000, v161
	v_pk_fma_f32 v[140:141], v[140:141], s[46:47], v[144:145] op_sel_hi:[1,0,1]
	v_pk_fma_f32 v[144:145], v[32:33], v[138:139], v[132:133] op_sel_hi:[1,0,1]
	v_pk_fma_f32 v[162:163], v[30:31], v[138:139], v[130:131] op_sel_hi:[1,0,1]
	s_nop 0
	v_min_f32_e32 v174, 0, v162
	v_mul_f32_e64 v138, |v162|, s33
	v_min_f32_e32 v175, 0, v163
	v_mul_f32_e64 v161, |v163|, s33
	v_min_f32_e32 v162, 0, v144
	v_mul_f32_e64 v144, |v144|, s33
	v_min_f32_e32 v163, 0, v145
	v_mul_f32_e64 v145, |v145|, s33
	v_exp_f32_e32 v144, v144
	v_exp_f32_e32 v145, v145
	v_exp_f32_e32 v138, v138
	v_exp_f32_e32 v161, v161
	v_add_f32_e32 v144, 1.0, v144
	v_add_f32_e32 v145, 1.0, v145
	v_add_f32_e32 v138, 1.0, v138
	v_add_f32_e32 v161, 1.0, v161
	v_log_f32_e32 v144, v144
	v_log_f32_e32 v145, v145
	v_log_f32_e32 v138, v138
	v_log_f32_e32 v161, v161
	v_xor_b32_e32 v144, 0x80000000, v144
	v_xor_b32_e32 v145, 0x80000000, v145
	v_pk_fma_f32 v[176:177], v[144:145], s[46:47], v[162:163] op_sel_hi:[1,0,1]
	v_xor_b32_e32 v145, 0x80000000, v161
	v_xor_b32_e32 v144, 0x80000000, v138
	v_pk_fma_f32 v[174:175], v[144:145], s[46:47], v[174:175] op_sel_hi:[1,0,1]
	v_add_u32_e32 v144, 0xa0, v160
	v_ashrrev_i32_e32 v145, 31, v144
	v_lshlrev_b64 v[144:145], 6, v[144:145]
	v_lshl_add_u64 v[144:145], s[24:25], 0, v[144:145]
	v_mul_f32_e32 v138, 0x3d800000, v139
	v_lshl_add_u64 v[144:145], v[144:145], 0, v[154:155]
	v_pk_fma_f32 v[134:135], v[10:11], v[138:139], v[134:135] op_sel_hi:[1,0,1]
	global_store_dwordx4 v[144:145], v[174:177], off
	global_store_dwordx4 v[144:145], v[140:143], off offset:16
	v_pk_fma_f32 v[136:137], v[12:13], v[138:139], v[136:137] op_sel_hi:[1,0,1]
	s_nop 0
	v_min_f32_e32 v140, 0, v134
	v_mul_f32_e64 v134, |v134|, s33
	v_exp_f32_e32 v134, v134
	v_min_f32_e32 v141, 0, v135
	v_add_f32_e32 v134, 1.0, v134
	v_log_f32_e32 v139, v134
	v_mul_f32_e64 v134, |v135|, s33
	v_mul_f32_e64 v135, |v136|, s33
	v_exp_f32_e32 v134, v134
	v_exp_f32_e32 v135, v135
	v_pk_fma_f32 v[130:131], v[14:15], v[138:139], v[130:131] op_sel_hi:[1,0,1]
	v_pk_fma_f32 v[132:133], v[16:17], v[138:139], v[132:133] op_sel_hi:[1,0,1]
	v_add_f32_e32 v134, 1.0, v134
	v_add_f32_e32 v135, 1.0, v135
	v_log_f32_e32 v142, v134
	v_min_f32_e32 v134, 0, v136
	v_log_f32_e32 v136, v135
	v_min_f32_e32 v135, 0, v137
	v_mul_f32_e64 v137, |v137|, s33
	v_exp_f32_e32 v137, v137
	v_min_f32_e32 v138, 0, v130
	v_mul_f32_e64 v130, |v130|, s33
	v_exp_f32_e32 v130, v130
	v_add_f32_e32 v137, 1.0, v137
	v_log_f32_e32 v137, v137
	v_xor_b32_e32 v136, 0x80000000, v136
	v_add_f32_e32 v130, 1.0, v130
	v_xor_b32_e32 v137, 0x80000000, v137
	v_pk_fma_f32 v[136:137], v[136:137], s[46:47], v[134:135] op_sel_hi:[1,0,1]
	v_xor_b32_e32 v135, 0x80000000, v142
	v_xor_b32_e32 v134, 0x80000000, v139
	v_pk_fma_f32 v[134:135], v[134:135], s[46:47], v[140:141] op_sel_hi:[1,0,1]
	v_log_f32_e32 v140, v130
	v_min_f32_e32 v139, 0, v131
	v_mul_f32_e64 v130, |v131|, s33
	v_mul_f32_e64 v131, |v132|, s33
	v_exp_f32_e32 v130, v130
	v_exp_f32_e32 v131, v131
	v_add_f32_e32 v130, 1.0, v130
	v_add_f32_e32 v131, 1.0, v131
	v_log_f32_e32 v141, v130
	v_min_f32_e32 v130, 0, v132
	v_log_f32_e32 v132, v131
	v_min_f32_e32 v131, 0, v133
	v_mul_f32_e64 v133, |v133|, s33
	v_exp_f32_e32 v133, v133
	v_xor_b32_e32 v132, 0x80000000, v132
	v_add_f32_e32 v133, 1.0, v133
	v_log_f32_e32 v133, v133
	s_nop 0
	v_xor_b32_e32 v133, 0x80000000, v133
	v_pk_fma_f32 v[132:133], v[132:133], s[46:47], v[130:131] op_sel_hi:[1,0,1]
	v_xor_b32_e32 v131, 0x80000000, v141
	v_xor_b32_e32 v130, 0x80000000, v140
	v_pk_fma_f32 v[130:131], v[130:131], s[46:47], v[138:139] op_sel_hi:[1,0,1]
	v_add_u32_e32 v138, 0xb0, v160
	v_ashrrev_i32_e32 v139, 31, v138
	v_lshlrev_b64 v[138:139], 6, v[138:139]
	v_lshl_add_u64 v[138:139], s[24:25], 0, v[138:139]
	v_lshl_add_u64 v[138:139], v[138:139], 0, v[154:155]
	global_store_dwordx4 v[138:139], v[130:133], off
	global_store_dwordx4 v[138:139], v[134:137], off offset:16
